# P10 loads nt
# speedup vs baseline: 1.0728x; 1.0337x over previous
.LBB0_1222:
	s_or_b64 exec, exec, s[0:1]
	v_cmp_lt_i32_e32 vcc, 0, v46
	s_and_saveexec_b64 s[0:1], vcc
	s_cbranch_execz .LBB0_1225
	v_mbcnt_lo_u32_b32 v0, -1, 0
	v_mbcnt_hi_u32_b32 v49, -1, v0
	v_lshlrev_b32_e32 v0, 2, v49
	v_and_b32_e32 v0, 0x100, v0
	ds_bpermute_b32 v2, v0, v47
	ds_bpermute_b32 v4, v0, v48
	s_add_u32 s0, s6, 0x4744a000
	s_addc_u32 s1, s7, 0
	s_add_u32 s8, s6, 0x2b80a000
	v_ashrrev_i32_e32 v33, 31, v32
	s_addc_u32 s9, s7, 0
	s_waitcnt lgkmcnt(1)
	v_ashrrev_i32_e32 v3, 31, v2
	s_waitcnt lgkmcnt(0)
	v_ashrrev_i32_e32 v5, 31, v4
	v_lshlrev_b64 v[6:7], 12, v[32:33]
	v_mov_b32_e32 v37, 0
	v_lshlrev_b64 v[2:3], 11, v[2:3]
	v_lshlrev_b64 v[4:5], 11, v[4:5]
	v_lshl_add_u64 v[6:7], s[8:9], 0, v[6:7]
	v_lshlrev_b32_e32 v42, 5, v1
	v_mov_b32_e32 v43, v37
	v_lshlrev_b32_e32 v36, 4, v1
	v_lshl_add_u64 v[2:3], s[0:1], 0, v[2:3]
	v_lshl_add_u64 v[4:5], s[0:1], 0, v[4:5]
	v_lshl_add_u64 v[44:45], v[6:7], 0, v[42:43]
	v_lshl_add_u64 v[38:39], v[2:3], 0, v[36:37]
	v_lshl_add_u64 v[40:41], v[4:5], 0, v[36:37]
	global_load_dwordx4 v[28:31], v[44:45], off nt
	global_load_dwordx4 v[16:19], v[44:45], off offset:16 nt
	global_load_dwordx4 v[20:23], v[38:39], off nt
	global_load_dwordx4 v[8:11], v[38:39], off offset:1024 nt
	global_load_dwordx4 v[24:27], v[40:41], off nt
	global_load_dwordx4 v[4:7], v[40:41], off offset:1024 nt
	global_load_dwordx4 v[12:15], v[44:45], off offset:2048 nt
	global_load_dwordx4 v[0:3], v[44:45], off offset:2064 nt
	v_or_b32_e32 v44, 0x400, v36
	s_mov_b32 s6, 0
	v_and_b32_e32 v33, 64, v49
	v_lshl_add_u64 v[38:39], s[0:1], 0, v[36:37]
	v_lshl_add_u64 v[40:41], s[8:9], 0, v[42:43]
	s_mov_b64 s[0:1], 0
	v_lshlrev_b32_e32 v36, 2, v36
	v_lshlrev_b32_e32 v42, 2, v44
	v_mov_b32_e32 v44, v32
.LBB0_1224:
	s_add_i32 s2, s6, 1
	v_mov_b32_e32 v50, s6
	s_waitcnt vmcnt(2)
	v_cvt_pk_f32_fp8_e32 v[134:135], v6
	v_cvt_pk_f32_fp8_sdwa v[136:137], v6 src0_sel:WORD_1
	v_mov_b32_e32 v6, s2
	v_cmp_lt_i32_e32 vcc, s2, v46
	v_and_or_b32 v49, s6, 63, v33
	s_waitcnt vmcnt(1)
	v_lshlrev_b32_e32 v118, 16, v12
	v_cndmask_b32_e32 v6, v50, v6, vcc
	v_and_b32_e32 v119, 0xffff0000, v12
	v_lshlrev_b32_e32 v120, 16, v13
	v_and_b32_e32 v121, 0xffff0000, v13
	v_mad_u64_u32 v[12:13], s[6:7], v6, s3, v[32:33]
	v_and_or_b32 v6, v6, 63, v33
	v_lshlrev_b32_e32 v6, 2, v6
	v_cvt_pk_f32_fp8_e32 v[66:67], v24
	v_cvt_pk_f32_fp8_sdwa v[68:69], v24 src0_sel:WORD_1
	v_cvt_pk_f32_fp8_e32 v[90:91], v26
	v_cvt_pk_f32_fp8_sdwa v[92:93], v26 src0_sel:WORD_1
	ds_bpermute_b32 v24, v6, v47
	ds_bpermute_b32 v26, v6, v48
	v_ashrrev_i32_e32 v13, 31, v12
	v_cvt_pk_f32_fp8_e32 v[78:79], v25
	v_cvt_pk_f32_fp8_sdwa v[80:81], v25 src0_sel:WORD_1
	v_cvt_pk_f32_fp8_e32 v[102:103], v27
	v_cvt_pk_f32_fp8_sdwa v[104:105], v27 src0_sel:WORD_1
	v_lshlrev_b64 v[12:13], 12, v[12:13]
	s_waitcnt lgkmcnt(1)
	v_ashrrev_i32_e32 v25, 31, v24
	s_waitcnt lgkmcnt(0)
	v_ashrrev_i32_e32 v27, 31, v26
	v_lshl_add_u64 v[50:51], v[40:41], 0, v[12:13]
	v_lshlrev_b64 v[24:25], 11, v[24:25]
	v_lshlrev_b64 v[26:27], 11, v[26:27]
	v_cvt_pk_f32_fp8_e32 v[62:63], v20
	v_cvt_pk_f32_fp8_sdwa v[64:65], v20 src0_sel:WORD_1
	v_lshlrev_b32_e32 v70, 16, v28
	v_and_b32_e32 v71, 0xffff0000, v28
	v_lshlrev_b32_e32 v72, 16, v29
	v_and_b32_e32 v73, 0xffff0000, v29
	v_cvt_pk_f32_fp8_e32 v[74:75], v21
	v_cvt_pk_f32_fp8_sdwa v[76:77], v21 src0_sel:WORD_1
	v_lshlrev_b32_e32 v82, 16, v30
	v_and_b32_e32 v83, 0xffff0000, v30
	v_lshlrev_b32_e32 v84, 16, v31
	v_and_b32_e32 v85, 0xffff0000, v31
	v_cvt_pk_f32_fp8_e32 v[86:87], v22
	v_cvt_pk_f32_fp8_sdwa v[88:89], v22 src0_sel:WORD_1
	v_lshlrev_b32_e32 v94, 16, v16
	v_and_b32_e32 v95, 0xffff0000, v16
	v_lshlrev_b32_e32 v96, 16, v17
	v_and_b32_e32 v97, 0xffff0000, v17
	v_cvt_pk_f32_fp8_e32 v[98:99], v23
	v_cvt_pk_f32_fp8_sdwa v[100:101], v23 src0_sel:WORD_1
	v_lshlrev_b32_e32 v106, 16, v18
	v_and_b32_e32 v107, 0xffff0000, v18
	v_lshlrev_b32_e32 v108, 16, v19
	v_and_b32_e32 v109, 0xffff0000, v19
	v_cvt_pk_f32_fp8_e32 v[114:115], v4
	v_cvt_pk_f32_fp8_sdwa v[116:117], v4 src0_sel:WORD_1
	v_cvt_pk_f32_fp8_e32 v[124:125], v5
	v_cvt_pk_f32_fp8_sdwa v[126:127], v5 src0_sel:WORD_1
	v_lshlrev_b32_e32 v4, 16, v14
	v_and_b32_e32 v5, 0xffff0000, v14
	v_lshlrev_b32_e32 v128, 16, v15
	v_and_b32_e32 v129, 0xffff0000, v15
	global_load_dwordx4 v[28:31], v[50:51], off nt
	global_load_dwordx4 v[16:19], v[50:51], off offset:16 nt
	global_load_dwordx4 v[12:15], v[50:51], off offset:2048 nt
	global_load_dwordx4 v[20:23], v[50:51], off offset:2064 nt
	v_lshl_add_u64 v[58:59], v[38:39], 0, v[24:25]
	v_lshl_add_u64 v[50:51], v[38:39], 0, v[26:27]
	global_load_dwordx4 v[24:27], v[50:51], off nt
	s_nop 0
	global_load_dwordx4 v[50:53], v[50:51], off offset:1024 nt
	s_nop 0
	global_load_dwordx4 v[54:57], v[58:59], off nt
	s_nop 0
	global_load_dwordx4 v[58:61], v[58:59], off offset:1024 nt
	v_lshlrev_b32_e32 v49, 2, v49
	ds_bpermute_b32 v148, v49, v34
	ds_bpermute_b32 v150, v49, v35
	v_cvt_pk_f32_fp8_e32 v[110:111], v8
	v_cvt_pk_f32_fp8_sdwa v[112:113], v8 src0_sel:WORD_1
	v_cvt_pk_f32_fp8_e32 v[122:123], v9
	v_cvt_pk_f32_fp8_sdwa v[8:9], v9 src0_sel:WORD_1
	v_cvt_pk_f32_fp8_e32 v[130:131], v10
	v_cvt_pk_f32_fp8_sdwa v[132:133], v10 src0_sel:WORD_1
	v_cvt_pk_f32_fp8_e32 v[140:141], v11
	v_cvt_pk_f32_fp8_sdwa v[10:11], v11 src0_sel:WORD_1
	v_ashrrev_i32_e32 v45, 31, v44
	v_cvt_pk_f32_fp8_e32 v[142:143], v7
	v_cvt_pk_f32_fp8_sdwa v[144:145], v7 src0_sel:WORD_1
	v_lshlrev_b64 v[146:147], 13, v[44:45]
	s_waitcnt vmcnt(8)
	v_lshlrev_b32_e32 v138, 16, v0
	v_and_b32_e32 v139, 0xffff0000, v0
	v_lshlrev_b32_e32 v0, 16, v1
	v_and_b32_e32 v1, 0xffff0000, v1
	v_lshlrev_b32_e32 v6, 16, v2
	v_and_b32_e32 v7, 0xffff0000, v2
	v_lshlrev_b32_e32 v2, 16, v3
	v_and_b32_e32 v3, 0xffff0000, v3
	v_lshl_add_u64 v[146:147], s[4:5], 0, v[146:147]
	s_waitcnt lgkmcnt(1)
	v_pk_fma_f32 v[62:63], v[62:63], v[148:149], v[70:71] op_sel_hi:[1,0,1]
	v_pk_fma_f32 v[64:65], v[64:65], v[148:149], v[72:73] op_sel_hi:[1,0,1]
	v_pk_fma_f32 v[70:71], v[74:75], v[148:149], v[82:83] op_sel_hi:[1,0,1]
	v_pk_fma_f32 v[72:73], v[76:77], v[148:149], v[84:85] op_sel_hi:[1,0,1]
	v_pk_fma_f32 v[74:75], v[86:87], v[148:149], v[94:95] op_sel_hi:[1,0,1]
	v_pk_fma_f32 v[76:77], v[88:89], v[148:149], v[96:97] op_sel_hi:[1,0,1]
	v_mov_b32_e32 v43, v37
	v_lshl_add_u64 v[152:153], v[146:147], 0, v[36:37]
	v_pk_fma_f32 v[82:83], v[98:99], v[148:149], v[106:107] op_sel_hi:[1,0,1]
	v_pk_fma_f32 v[84:85], v[100:101], v[148:149], v[108:109] op_sel_hi:[1,0,1]
	v_pk_fma_f32 v[86:87], v[110:111], v[148:149], v[118:119] op_sel_hi:[1,0,1]
	v_pk_fma_f32 v[88:89], v[112:113], v[148:149], v[120:121] op_sel_hi:[1,0,1]
	v_pk_fma_f32 v[94:95], v[122:123], v[148:149], v[4:5] op_sel_hi:[1,0,1]
	v_pk_fma_f32 v[96:97], v[8:9], v[148:149], v[128:129] op_sel_hi:[1,0,1]
	v_pk_fma_f32 v[98:99], v[130:131], v[148:149], v[138:139] op_sel_hi:[1,0,1]
	v_pk_fma_f32 v[100:101], v[132:133], v[148:149], v[0:1] op_sel_hi:[1,0,1]
	v_pk_fma_f32 v[106:107], v[140:141], v[148:149], v[6:7] op_sel_hi:[1,0,1]
	v_pk_fma_f32 v[108:109], v[10:11], v[148:149], v[2:3] op_sel_hi:[1,0,1]
	s_waitcnt lgkmcnt(0)
	v_pk_fma_f32 v[0:1], v[66:67], v[150:151], v[62:63] op_sel_hi:[1,0,1]
	v_pk_fma_f32 v[2:3], v[68:69], v[150:151], v[64:65] op_sel_hi:[1,0,1]
	v_pk_fma_f32 v[4:5], v[78:79], v[150:151], v[70:71] op_sel_hi:[1,0,1]
	v_pk_fma_f32 v[6:7], v[80:81], v[150:151], v[72:73] op_sel_hi:[1,0,1]
	v_pk_fma_f32 v[8:9], v[90:91], v[150:151], v[74:75] op_sel_hi:[1,0,1]
	v_pk_fma_f32 v[10:11], v[92:93], v[150:151], v[76:77] op_sel_hi:[1,0,1]
	v_cmp_eq_u32_e32 vcc, s2, v46
	v_lshl_add_u64 v[146:147], v[146:147], 0, v[42:43]
	v_pk_fma_f32 v[62:63], v[102:103], v[150:151], v[82:83] op_sel_hi:[1,0,1]
	v_pk_fma_f32 v[64:65], v[104:105], v[150:151], v[84:85] op_sel_hi:[1,0,1]
	v_pk_fma_f32 v[66:67], v[114:115], v[150:151], v[86:87] op_sel_hi:[1,0,1]
	v_pk_fma_f32 v[68:69], v[116:117], v[150:151], v[88:89] op_sel_hi:[1,0,1]
	v_pk_fma_f32 v[70:71], v[124:125], v[150:151], v[94:95] op_sel_hi:[1,0,1]
	v_pk_fma_f32 v[72:73], v[126:127], v[150:151], v[96:97] op_sel_hi:[1,0,1]
	v_pk_fma_f32 v[74:75], v[134:135], v[150:151], v[98:99] op_sel_hi:[1,0,1]
	v_pk_fma_f32 v[76:77], v[136:137], v[150:151], v[100:101] op_sel_hi:[1,0,1]
	v_pk_fma_f32 v[78:79], v[142:143], v[150:151], v[106:107] op_sel_hi:[1,0,1]
	v_pk_fma_f32 v[80:81], v[144:145], v[150:151], v[108:109] op_sel_hi:[1,0,1]
	global_store_dwordx4 v[152:153], v[0:3], off
	global_store_dwordx4 v[152:153], v[4:7], off offset:16
	global_store_dwordx4 v[152:153], v[8:11], off offset:32
	global_store_dwordx4 v[152:153], v[62:65], off offset:48
	global_store_dwordx4 v[146:147], v[66:69], off
	global_store_dwordx4 v[146:147], v[70:73], off offset:16
	global_store_dwordx4 v[146:147], v[74:77], off offset:32
	global_store_dwordx4 v[146:147], v[78:81], off offset:48
	v_add_u32_e32 v44, s3, v44
	s_mov_b32 s6, s2
	s_or_b64 s[0:1], vcc, s[0:1]
	s_waitcnt vmcnt(12)
	v_mov_b32_e32 v0, v20
	v_mov_b32_e32 v1, v21
	v_mov_b32_e32 v2, v22
	v_mov_b32_e32 v3, v23
	s_waitcnt vmcnt(10)
	v_mov_b64_e32 v[4:5], v[50:51]
	s_waitcnt vmcnt(9)
	v_mov_b64_e32 v[20:21], v[54:55]
	s_waitcnt vmcnt(8)
	v_mov_b64_e32 v[8:9], v[58:59]
	v_mov_b64_e32 v[6:7], v[52:53]
	v_mov_b64_e32 v[22:23], v[56:57]
	v_mov_b64_e32 v[10:11], v[60:61]
	s_andn2_b64 exec, exec, s[0:1]
	s_cbranch_execnz .LBB0_1224
